# t7_ld_sc1nt
# speedup vs baseline: 1.0598x; 1.0598x over previous
_Z11align_fusedPKfS0_PKiPf:
	s_load_dwordx2 s[6:7], s[0:1], 0x0
	s_sub_u32 s2, 0x1fff, s2
	s_mul_hi_u32 s3, s2, 0x1770
	s_mulk_i32 s2, 0x1770
	s_lshl_b64 s[4:5], s[2:3], 2
	s_waitcnt lgkmcnt(0)
	s_add_u32 s2, s6, s4
	s_addc_u32 s3, s7, s5
	v_mov_b32_e32 v31, 0
	v_lshlrev_b32_e32 v30, 4, v0
	v_lshl_add_u64 v[10:11], s[2:3], 0, v[30:31]
	s_movk_i32 s7, 0x2000
	v_add_co_u32_e32 v12, vcc, s7, v10
	s_movk_i32 s7, 0x3000
	s_nop 0
	v_addc_co_u32_e32 v13, vcc, 0, v11, vcc
	v_add_co_u32_e32 v18, vcc, s7, v10
	s_movk_i32 s6, 0xdc
	s_nop 0
	v_addc_co_u32_e32 v19, vcc, 0, v11, vcc
	v_add_co_u32_e32 v20, vcc, 0x4000, v10
	v_or_b32_e32 v48, 0x400, v0
	s_nop 0
	v_addc_co_u32_e32 v21, vcc, 0, v11, vcc
	v_or_b32_e32 v1, 0x500, v0
	v_cmp_gt_u32_e32 vcc, s6, v0
	global_load_dwordx4 v[2:5], v[12:13], off offset:-4096 sc1 nt
	global_load_dwordx4 v[6:9], v[12:13], off sc1 nt
	v_cndmask_b32_e32 v1, v48, v1, vcc
	global_load_dwordx4 v[10:13], v[18:19], off sc1 nt
	global_load_dwordx4 v[14:17], v[20:21], off sc1 nt
	v_lshlrev_b32_e32 v49, 4, v1
	global_load_dwordx4 v[22:25], v30, s[2:3] sc1 nt
	global_load_dwordx4 v[18:21], v49, s[2:3] sc1 nt
	v_and_b32_e32 v29, 63, v0
	v_cmp_gt_u32_e32 vcc, 64, v0
	v_mov_b32_e32 v26, v31
	v_mov_b32_e32 v27, v31
	v_mov_b32_e32 v28, v31
	s_and_saveexec_b64 s[2:3], vcc
	s_cbranch_execz .LBB0_2
	s_load_dwordx4 s[8:11], s[0:1], 0x8
	v_mul_u32_u24_e32 v1, 3, v29
	v_lshlrev_b32_e32 v31, 2, v29
	v_lshlrev_b32_e32 v1, 2, v1
	s_waitcnt lgkmcnt(0)
	global_load_dword v32, v31, s[10:11]
	global_load_dwordx3 v[26:28], v1, s[8:9] nt
	s_waitcnt vmcnt(1)
	v_lshl_add_u32 v31, v32, 1, v32
